# diff attention: all 8 waves in the same role; row-sum adds of the softmax moved behind the mid-tile barrier (rebalances QK/softmax vs PV phases)
# speedup vs baseline: 1.0247x; 1.0060x over previous
; #define VMW() asm volatile("s_waitcnt vmcnt(0)" ::: "memory")
; #define WLOADK(k0, par) do { if constexpr (VAR == 4) { if ((k0) > 0) break; } const size_t tb_ = (VAR == 5) ? (size_t)0 : (size_t)(k0) * D;                                            \
;         __builtin_amdgcn_global_load_lds((const unsigned*)(Kh + tb_ + koff), (lds_uptr)(K_lds + (par) * SHM_K + wid * 1024), 16, 0, 0); } while (0)
; #define WLOADK(t_, par) __builtin_amdgcn_global_load_lds((const unsigned*)(Kh + (size_t)(t_) * (KVBLK * D) + koff), (lds_uptr)(K_lds + (par) * SHM_K + wid * 1024), 16, 0, 0)
; template <class Epi>
; __device__ __forceinline__ void block_wide8(const BlockRef& cur, const bf16* V2, int skv, char* lds, Seam& S, const Epi& E) {
;     int tid = threadIdx.x; asm volatile("" : "+v"(tid));
;     const int wid = __builtin_amdgcn_readfirstlane(tid >> 6), lane = tid & 63, r32 = lane & 31, hi = lane >> 5;
;     int j_hi = (cur.P0 + QB - 1) / KVBLK + 1; if (j_hi > skv / KVBLK) j_hi = skv / KVBLK;
;     const int NT = j_hi;
;     const int qlo = cur.P0 + wid * QBLK, qm = qlo + r32 - 8 * hi;
;     char* V_lds = lds; char* K_lds = lds + 4 * SHM_V;
;     float* ws = (float*)(lds + WIDE_WS) + wid * 64; float* li_l = ws, * al_l = ws + 32;
;     float m_reg = -1e30f, l_reg = 0; f32x16 o[8] = {};
;     const int krow = 8 * wid + (lane >> 3), krp = krow & 31, kt = (krp & 3) + 4 * (krp >> 3) + 16 * (krow >> 5), kkey = 16 * (kt & 3) + (kt >> 2) + 8 * ((krp >> 2) & 1);
;     const unsigned koff = (unsigned)(kkey * 128 + (((lane & 7) ^ ((krow >> 1) & 7)) << 4));
;     const int vc = 16 * wid + (lane >> 2);
;     const unsigned voff = (unsigned)(vc * 64 + (((lane & 3) ^ ((vc >> 2) & 3)) << 4));
;     const char* Kh = (const char*)cur.K; const char* Va = (const char*)cur.V; const char* Vb = (const char*)V2;
;     typedef __attribute__((address_space(3))) unsigned* lds_uptr;
;     ...
;     i32x8 q8[2];
;     { const i32x4* qp = (const i32x4*)((const char*)cur.Q + (size_t)(wid * QBLK + r32) * D + hi * 32);
; #pragma unroll
;       for (int c = 0; c < 2; ++c) { const i32x4 lo_ = qp[4 * c], hi_ = qp[4 * c + 1]; q8[c] = (i32x8){lo_[0], lo_[1], lo_[2], lo_[3], hi_[0], hi_[1], hi_[2], hi_[3]}; } }
;     WLOADK(0, 0); WLOADV(0, 0); VMW();
;     __syncthreads();
;     ...
;     if (wid < 4) {
.LBB0_1199:
	s_and_b64 vcc, exec, s[4:5]
	s_cbranch_vccz .LBB0_973
	s_bfe_u32 s16, s29, 0x20003
	s_and_b32 s15, s29, 7
	s_lshl_b32 s17, s16, 4
	s_lshl_b32 s19, s15, 1
	s_or_b32 s8, s17, s19
	s_lshl_b32 s6, s29, 3
	s_add_i32 s4, s8, s30
	s_and_b32 s10, s6, 0xffffff00
	s_ashr_i32 s5, s4, 31
	s_sub_i32 s86, 0xf00, s10
	s_lshl_b64 s[4:5], s[4:5], 19
	s_lshl_b64 s[6:7], s[86:87], 7
	v_readlane_b32 s9, v252, 14
	s_add_u32 s9, s9, s4
	v_readlane_b32 s11, v252, 15
	s_addc_u32 s11, s11, s5
	s_add_u32 s6, s9, s6
	s_addc_u32 s7, s11, s7
	v_readlane_b32 s9, v252, 16
	s_add_u32 s4, s9, s4
	v_readlane_b32 s9, v252, 17
	s_addc_u32 s5, s9, s5
	s_lshl_b32 s8, s8, 19
	v_readlane_b32 s9, v252, 18
	s_add_u32 s8, s9, s8
	v_readlane_b32 s9, v252, 23
	s_addc_u32 s9, s9, 0
	s_sub_i32 s10, 0xfff, s10
	v_mov_b32_e32 v6, v0
	s_ashr_i32 s13, s10, 31
	s_lshr_b32 s13, s13, 26
	v_readfirstlane_b32 s11, v6
	s_add_i32 s10, s10, s13
	s_and_b32 s13, s11, 0x3fffffc0
	s_ashr_i32 s12, s11, 6
	s_lshl_b32 s13, s13, 2
	s_add_i32 s93, s13, 0
	s_lshl_b32 s13, s12, 2
	s_ashr_i32 s11, s11, 4
	v_bfe_u32 v4, v6, 4, 2
	s_and_b32 s14, s13, 12
	s_and_b32 s11, s11, -16
	v_lshlrev_b32_e32 v2, 1, v6
	v_lshrrev_b32_e32 v7, 2, v6
	v_bitop3_b32 v4, v4, v6, s13 bitop3:0x36
	v_and_b32_e32 v202, 31, v6
	s_ashr_i32 s10, s10, 6
	s_lshl_b32 s18, s12, 5
	s_or_b32 s11, s14, s11
	v_and_b32_e32 v217, 48, v2
	v_and_b32_e32 v218, 8, v7
	v_lshlrev_b32_e32 v4, 4, v4
	s_add_i32 s93, s93, 0x18000
	s_ashr_i32 s11, s11, 2
	v_or_b32_e32 v2, v217, v218
	v_and_b32_e32 v219, 0x70, v4
	v_or_b32_e32 v4, s18, v202
	s_add_i32 s10, s10, 1
	v_add_u32_e32 v2, s11, v2
	v_ashrrev_i32_e32 v5, 31, v4
	s_cmpk_lt_i32 s86, 0xf01
	v_lshl_or_b32 v8, v2, 7, v219
	v_lshlrev_b32_e32 v2, 4, v6
	v_lshlrev_b64 v[4:5], 7, v[4:5]
	s_cselect_b32 s79, s10, 64
	s_lshl_b32 s72, s12, 10
	v_and_b32_e32 v220, 0x3c0, v2
	v_bitop3_b32 v221, v2, 48, v6 bitop3:0x48
	v_lshl_add_u64 v[4:5], s[6:7], 0, v[4:5]
	v_and_b32_e32 v2, 32, v6
	s_add_i32 s85, s72, 0
	v_lshl_add_u64 v[4:5], v[4:5], 0, v[2:3]
	s_add_i32 s89, s85, 0x10000
	global_load_dwordx4 v[182:185], v[4:5], off offset:16
	global_load_dwordx4 v[178:181], v[4:5], off
	global_load_dwordx4 v[190:193], v[4:5], off offset:80
	global_load_dwordx4 v[186:189], v[4:5], off offset:64
	v_or3_b32 v2, v220, v221, s72
	s_mov_b32 m0, s89
	v_lshl_add_u64 v[4:5], s[8:9], 0, v[2:3]
	global_load_lds_dwordx4 v8, s[4:5]
	s_mov_b32 m0, s85
	s_mov_b64 s[4:5], 0x80000
	s_add_i32 s81, s85, 0x4000
	global_load_lds_dwordx4 v2, s[8:9]
	v_lshl_add_u64 v[4:5], v[4:5], 0, s[4:5]
	s_mov_b32 m0, s81
	v_bfe_u32 v213, v6, 5, 1
	global_load_lds_dwordx4 v[4:5], off
	s_mov_b32 s4, s18
	s_add_i32 s80, s18, s86
	v_lshlrev_b32_e32 v2, 3, v213
	v_writelane_b32 v252, s4, 38
	s_cmp_lg_u32 0, -1
	v_sub_u32_e32 v2, v202, v2
	v_writelane_b32 v252, s5, 39
	s_cselect_b32 s4, 0, 0
	s_cmp_gt_i32 s79, 0
	v_add_u32_e32 v201, s80, v2
	s_waitcnt vmcnt(0)
	v_bfe_u32 v2, v6, 2, 2
	v_lshl_add_u32 v4, v202, 6, s4
	v_lshlrev_b32_e32 v5, 1, v213
	s_cselect_b64 s[4:5], -1, 0
	v_and_b32_e32 v200, 63, v6
	v_bitop3_b32 v6, v5, v7, 3 bitop3:0x78
	v_bitop3_b32 v2, v5, v2, 1 bitop3:0x36
	v_writelane_b32 v252, s4, 40
	s_cmp_lt_i32 s79, 1
	s_mov_b32 s77, s29
	v_lshl_add_u32 v203, v6, 4, v4
	v_lshl_add_u32 v214, v2, 4, v4
	v_writelane_b32 v252, s5, 41
	s_cselect_b64 s[6:7], -1, 0
	s_cmp_lt_i32 s12, 8
	s_mov_b64 s[4:5], -1
	s_waitcnt vmcnt(0) lgkmcnt(0)
	s_barrier
	s_cbranch_scc1 .LBB0_1247
	s_andn2_b64 vcc, exec, s[6:7]
	v_add_u32_e32 v222, 0x8000, v203
	v_add_u32_e32 v223, 0x8000, v214
	v_add_u32_e32 v224, 0x8800, v203
	v_add_u32_e32 v225, 0x8800, v214
	v_add_u32_e32 v226, 0x9000, v203
	v_add_u32_e32 v227, 0x9000, v214
	v_add_u32_e32 v228, 0x9800, v203
	v_add_u32_e32 v229, 0x9800, v214
	v_add_u32_e32 v230, 0xc000, v203
	v_add_u32_e32 v231, 0xc000, v214
	v_add_u32_e32 v232, 0xc800, v203
	v_add_u32_e32 v233, 0xc800, v214
	v_add_u32_e32 v234, 0xd000, v203
	v_add_u32_e32 v235, 0xd000, v214
	v_add_u32_e32 v236, 0xd800, v203
	v_add_u32_e32 v237, 0xd800, v214
	s_cbranch_vccnz .LBB0_1203
	v_add_u32_e32 v168, 0x8000, v203
	v_add_u32_e32 v169, 0x8000, v214
	v_add_u32_e32 v166, 0x8800, v203
	v_add_u32_e32 v167, 0x8800, v214
	v_add_u32_e32 v164, 0x9000, v203
	v_add_u32_e32 v165, 0x9000, v214
	v_add_u32_e32 v162, 0x9800, v203
	v_add_u32_e32 v163, 0x9800, v214
	v_add_u32_e32 v160, 0xc000, v203
	v_add_u32_e32 v161, 0xc000, v214
	v_add_u32_e32 v158, 0xc800, v203
	v_add_u32_e32 v159, 0xc800, v214
	v_add_u32_e32 v156, 0xd000, v203
	v_add_u32_e32 v157, 0xd000, v214
	v_add_u32_e32 v154, 0xd800, v203
	v_add_u32_e32 v155, 0xd800, v214
	s_mov_b64 s[4:5], 0

;     ...
;     constexpr float SCL = SCALE / (float)(1 << SH), C2 = 1.4426950408889634f * SCL;
;     if (__builtin_expect(__all((pmax - m_reg) * SCL <= (float)THRI), 1)) { mn = m_reg; alpha = 1.f; }
;     else { mn = fmaxf(m_reg, pmax); alpha = __builtin_amdgcn_exp2f((m_reg - mn) * C2); m_reg = mn; }
;     const float mnL = dead ? -__builtin_inff() : -mn * C2 + (float)PSH;
;     for (int r = 0; r < 16; ++r) p0[r] = fmaf(p0[r], C2, mnL); for (int r = 0; r < 16; ++r) p1[r] = fmaf(p1[r], C2, mnL);
;     for (int r = 0; r < 16; ++r) p0[r] = __builtin_amdgcn_exp2f(p0[r]);
; }
; __device__ __forceinline__ void finishSM(f32x16& p0, f32x16& p1, float alpha, float& l_reg, bf16x8& pa0, bf16x8& pa1, bf16x8& pa2, bf16x8& pa3) {
;     for (int r = 0; r < 16; ++r) p1[r] = __builtin_amdgcn_exp2f(p1[r]);
.LBB0_1259:
	v_cndmask_b32_e64 v219, v16, v219, s[6:7]
	v_fmamk_f32 v16, v219, 0xba0293ee, v1
	v_fmamk_f32 v4, v162, 0x3a0293ee, v16
	v_fmamk_f32 v5, v163, 0x3a0293ee, v16
	v_fmamk_f32 v6, v164, 0x3a0293ee, v16
	v_fmamk_f32 v7, v165, 0x3a0293ee, v16
	v_fmamk_f32 v8, v166, 0x3a0293ee, v16
	v_fmamk_f32 v164, v173, 0x3a0293ee, v16
	v_fmamk_f32 v165, v174, 0x3a0293ee, v16
	v_fmamk_f32 v146, v146, 0x3a0293ee, v16
	v_fmamk_f32 v147, v147, 0x3a0293ee, v16
	v_fmamk_f32 v148, v148, 0x3a0293ee, v16
	v_fmamk_f32 v149, v149, 0x3a0293ee, v16
	v_fmamk_f32 v9, v167, 0x3a0293ee, v16
	v_fmamk_f32 v11, v168, 0x3a0293ee, v16
	v_fmamk_f32 v13, v169, 0x3a0293ee, v16
	v_fmamk_f32 v162, v171, 0x3a0293ee, v16
	v_fmamk_f32 v163, v172, 0x3a0293ee, v16
	v_fmamk_f32 v166, v175, 0x3a0293ee, v16
	v_fmamk_f32 v167, v176, 0x3a0293ee, v16
	v_fmamk_f32 v169, v150, 0x3a0293ee, v16
	v_fmamk_f32 v152, v152, 0x3a0293ee, v16
	v_fmamk_f32 v171, v154, 0x3a0293ee, v16
	v_fmamk_f32 v172, v155, 0x3a0293ee, v16
	v_fmamk_f32 v175, v158, 0x3a0293ee, v16
	v_fmamk_f32 v176, v159, 0x3a0293ee, v16
	v_exp_f32_e32 v154, v4
	v_exp_f32_e32 v155, v5
	v_exp_f32_e32 v10, v6
	v_exp_f32_e32 v12, v7
	v_exp_f32_e32 v150, v8
	v_exp_f32_e32 v5, v164
	v_exp_f32_e32 v8, v165
	v_exp_f32_e32 v164, v146
	v_exp_f32_e32 v165, v147
	v_exp_f32_e32 v158, v148
	v_exp_f32_e32 v159, v149
	v_fmamk_f32 v17, v170, 0x3a0293ee, v16
	v_fmamk_f32 v168, v177, 0x3a0293ee, v16
	v_fmamk_f32 v170, v151, 0x3a0293ee, v16
	v_fmamk_f32 v153, v153, 0x3a0293ee, v16
	v_fmamk_f32 v177, v160, 0x3a0293ee, v16
	v_exp_f32_e32 v14, v11
	v_exp_f32_e32 v15, v13
	v_exp_f32_e32 v13, v162
	v_exp_f32_e32 v162, v169
	v_exp_f32_e32 v160, v152
	v_fmamk_f32 v173, v156, 0x3a0293ee, v16
	v_fmamk_f32 v174, v157, 0x3a0293ee, v16
	v_fmac_f32_e32 v16, 0x3a0293ee, v161
	v_exp_f32_e32 v151, v9
	v_exp_f32_e32 v4, v163
	v_exp_f32_e32 v163, v170
	v_exp_f32_e32 v161, v153
	v_exp_f32_e32 v11, v17
	v_exp_f32_e32 v156, v171
	v_exp_f32_e32 v146, v173
	v_exp_f32_e32 v9, v166
	v_exp_f32_e32 v6, v167
	v_exp_f32_e32 v157, v172
	v_exp_f32_e32 v147, v174
	v_exp_f32_e32 v149, v16
	v_exp_f32_e32 v152, v175
	v_exp_f32_e32 v148, v177
	v_exp_f32_e32 v7, v168
	v_exp_f32_e32 v153, v176
	s_setprio 0
	s_mov_b64 s[6:7], -1
	s_and_b64 vcc, exec, s[70:71]
	s_cbranch_vccz .LBB0_1261
	s_waitcnt vmcnt(0) lgkmcnt(0)
	s_mov_b64 s[6:7], 0

; __device__ __forceinline__ void finishSM8(f32x16& p0, f32x16& p1, float alpha, float& l_reg, i32x8& pa) {
;     for (int r = 0; r < 16; ++r) p1[r] = __builtin_amdgcn_exp2f(p1[r]);
;     float ps;
;     { float s0 = p0[0] + p0[1], s1 = p0[2] + p0[3], s2 = p1[0] + p1[1], s3 = p1[2] + p1[3];
; #pragma unroll
;       for (int r = 4; r < 16; r += 4) { s0 += p0[r]; s0 += p0[r + 1]; s1 += p0[r + 2]; s1 += p0[r + 3]; s2 += p1[r]; s2 += p1[r + 1]; s3 += p1[r + 2]; s3 += p1[r + 3]; }
;       ps = (s0 + s1) + (s2 + s3); }
;     { auto rr = __builtin_amdgcn_permlane32_swap(__float_as_uint(ps), __float_as_uint(ps), false, false);
;       ps = __uint_as_float(rr[0]) + __uint_as_float(rr[1]); }
;     l_reg = l_reg * alpha + ps;
; #pragma unroll
;     for (int d = 0; d < 4; ++d) { int w0 = 0, w1 = 0;
;         w0 = __builtin_amdgcn_cvt_pk_fp8_f32(p0[4 * d], p0[4 * d + 1], w0, false); w0 = __builtin_amdgcn_cvt_pk_fp8_f32(p0[4 * d + 2], p0[4 * d + 3], w0, true);
;         w1 = __builtin_amdgcn_cvt_pk_fp8_f32(p1[4 * d], p1[4 * d + 1], w1, false); w1 = __builtin_amdgcn_cvt_pk_fp8_f32(p1[4 * d + 2], p1[4 * d + 3], w1, true);
;         pa[d] = w0; pa[4 + d] = w1; }
.LBB0_1265:
	v_add_f32_e32 v254, v154, v155
	v_add_f32_e32 v255, v10, v12
	v_add_f32_e32 v166, v164, v165
	v_add_f32_e32 v167, v158, v159
	v_add_f32_e32 v254, v150, v254
	v_add_f32_e32 v255, v14, v255
	v_add_f32_e32 v166, v162, v166
	v_add_f32_e32 v167, v160, v167
	v_add_f32_e32 v254, v151, v254
	v_add_f32_e32 v255, v15, v255
	v_add_f32_e32 v166, v163, v166
	v_add_f32_e32 v167, v161, v167
	v_add_f32_e32 v254, v11, v254
	v_add_f32_e32 v255, v4, v255
	v_add_f32_e32 v166, v156, v166
	v_add_f32_e32 v167, v146, v167
	v_add_f32_e32 v254, v13, v254
	v_add_f32_e32 v255, v5, v255
	v_add_f32_e32 v166, v157, v166
	v_add_f32_e32 v167, v147, v167
	v_add_f32_e32 v254, v8, v254
	v_add_f32_e32 v255, v6, v255
	v_add_f32_e32 v166, v152, v166
	v_add_f32_e32 v167, v148, v167
	v_add_f32_e32 v254, v9, v254
	v_add_f32_e32 v255, v7, v255
	v_add_f32_e32 v166, v153, v166
	v_add_f32_e32 v167, v149, v167
	v_add_f32_e32 v254, v255, v254
	v_add_f32_e32 v255, v166, v167
	v_add_f32_e32 v217, v255, v254
	v_mov_b32_e32 v218, v217
	s_nop 1
	v_permlane32_swap_b32_e32 v217, v218
	v_mov_b32_e32 v166, 0
	v_mov_b32_e32 v170, 0
	v_mov_b32_e32 v167, 0
	v_mov_b32_e32 v171, 0
	v_mov_b32_e32 v168, 0
	v_mov_b32_e32 v172, 0
	v_mov_b32_e32 v169, 0
	v_mov_b32_e32 v173, 0
	v_cvt_pk_fp8_f32 v166, v154, v155
	v_cvt_pk_fp8_f32 v170, v164, v165
	v_cvt_pk_fp8_f32 v167, v150, v151
	v_cvt_pk_fp8_f32 v171, v162, v163
	v_cvt_pk_fp8_f32 v168, v11, v13
	v_cvt_pk_fp8_f32 v172, v156, v157
	v_cvt_pk_fp8_f32 v169, v8, v9
	v_cvt_pk_fp8_f32 v173, v152, v153
	v_cvt_pk_fp8_f32 v166, v10, v12 op_sel:[0,0,1]
	v_cvt_pk_fp8_f32 v170, v158, v159 op_sel:[0,0,1]
	v_cvt_pk_fp8_f32 v167, v14, v15 op_sel:[0,0,1]
	v_cvt_pk_fp8_f32 v171, v160, v161 op_sel:[0,0,1]
	v_cvt_pk_fp8_f32 v168, v4, v5 op_sel:[0,0,1]
	v_cvt_pk_fp8_f32 v172, v146, v147 op_sel:[0,0,1]
	v_cvt_pk_fp8_f32 v169, v6, v7 op_sel:[0,0,1]
	v_cvt_pk_fp8_f32 v173, v148, v149 op_sel:[0,0,1]
	ds_read_b128 v[4:7], v203
	ds_read_b128 v[146:149], v203 offset:2048
	ds_read_b128 v[8:11], v214
	ds_read_b128 v[150:153], v214 offset:2048
	s_waitcnt lgkmcnt(0)
	v_mfma_f32_32x32x64_f8f6f4 v[130:145], v[166:173], v[4:11], v[130:145]
	ds_read_b128 v[4:7], v203 offset:4096
	ds_read_b128 v[8:11], v214 offset:4096
	v_mfma_f32_32x32x64_f8f6f4 v[114:129], v[166:173], v[146:153], v[114:129]
	ds_read_b128 v[146:149], v203 offset:6144
	ds_read_b128 v[150:153], v214 offset:6144
	s_waitcnt lgkmcnt(0)
	v_mfma_f32_32x32x64_f8f6f4 v[98:113], v[166:173], v[4:11], v[98:113]
	ds_read_b128 v[4:7], v203 offset:16384
	ds_read_b128 v[8:11], v214 offset:16384
	v_mfma_f32_32x32x64_f8f6f4 v[82:97], v[166:173], v[146:153], v[82:97]
	ds_read_b128 v[146:149], v203 offset:18432
	ds_read_b128 v[150:153], v214 offset:18432
	s_waitcnt lgkmcnt(0)
	v_mfma_f32_32x32x64_f8f6f4 v[66:81], v[166:173], v[4:11], v[66:81]
	ds_read_b128 v[4:7], v203 offset:20480
	ds_read_b128 v[8:11], v214 offset:20480
	v_mfma_f32_32x32x64_f8f6f4 v[50:65], v[166:173], v[146:153], v[50:65]
	ds_read_b128 v[146:149], v203 offset:22528
	ds_read_b128 v[150:153], v214 offset:22528
	s_waitcnt lgkmcnt(0)
	v_mfma_f32_32x32x64_f8f6f4 v[34:49], v[166:173], v[4:11], v[34:49]
	v_mfma_f32_32x32x64_f8f6f4 v[18:33], v[166:173], v[146:153], v[18:33]
	s_nop 15
	s_nop 15
	s_mov_b64 s[6:7], -1
	s_and_b64 vcc, exec, s[70:71]
	s_cbranch_vccz .LBB0_1267
	s_waitcnt vmcnt(0) lgkmcnt(0)
	s_mov_b64 s[6:7], 0

;     ...
;     constexpr float SCL = SCALE / (float)(1 << SH), C2 = 1.4426950408889634f * SCL;
;     if (__builtin_expect(__all((pmax - m_reg) * SCL <= (float)THRI), 1)) { mn = m_reg; alpha = 1.f; }
;     else { mn = fmaxf(m_reg, pmax); alpha = __builtin_amdgcn_exp2f((m_reg - mn) * C2); m_reg = mn; }
;     const float mnL = dead ? -__builtin_inff() : -mn * C2 + (float)PSH;
;     for (int r = 0; r < 16; ++r) p0[r] = fmaf(p0[r], C2, mnL); for (int r = 0; r < 16; ++r) p1[r] = fmaf(p1[r], C2, mnL);
;     for (int r = 0; r < 16; ++r) p0[r] = __builtin_amdgcn_exp2f(p0[r]);
; }
; __device__ __forceinline__ void finishSM(f32x16& p0, f32x16& p1, float alpha, float& l_reg, bf16x8& pa0, bf16x8& pa1, bf16x8& pa2, bf16x8& pa3) {
;     for (int r = 0; r < 16; ++r) p1[r] = __builtin_amdgcn_exp2f(p1[r]);
.LBB0_1277:
	v_cndmask_b32_e64 v219, v209, v219, s[6:7]
	v_fmamk_f32 v4, v219, 0xba0293ee, v1
	v_fmamk_f32 v5, v162, 0x3a0293ee, v4
	v_fmamk_f32 v6, v163, 0x3a0293ee, v4
	v_fmamk_f32 v7, v164, 0x3a0293ee, v4
	v_fmamk_f32 v8, v165, 0x3a0293ee, v4
	v_fmamk_f32 v9, v166, 0x3a0293ee, v4
	v_fmamk_f32 v10, v167, 0x3a0293ee, v4
	v_fmamk_f32 v11, v168, 0x3a0293ee, v4
	v_fmamk_f32 v13, v169, 0x3a0293ee, v4
	v_fmamk_f32 v15, v170, 0x3a0293ee, v4
	v_fmamk_f32 v166, v175, 0x3a0293ee, v4
	v_fmamk_f32 v167, v176, 0x3a0293ee, v4
	v_fmamk_f32 v169, v146, 0x3a0293ee, v4
	v_fmamk_f32 v170, v147, 0x3a0293ee, v4
	v_fmamk_f32 v148, v148, 0x3a0293ee, v4
	v_fmamk_f32 v149, v149, 0x3a0293ee, v4
	v_fmamk_f32 v162, v171, 0x3a0293ee, v4
	v_fmamk_f32 v163, v172, 0x3a0293ee, v4
	v_fmamk_f32 v164, v173, 0x3a0293ee, v4
	v_fmamk_f32 v165, v174, 0x3a0293ee, v4
	v_fmamk_f32 v168, v177, 0x3a0293ee, v4
	v_fmamk_f32 v150, v150, 0x3a0293ee, v4
	v_fmamk_f32 v151, v151, 0x3a0293ee, v4
	v_fmamk_f32 v171, v152, 0x3a0293ee, v4
	v_fmamk_f32 v172, v153, 0x3a0293ee, v4
	v_fmamk_f32 v154, v154, 0x3a0293ee, v4
	v_fmamk_f32 v155, v155, 0x3a0293ee, v4
	v_fmamk_f32 v173, v156, 0x3a0293ee, v4
	v_fmamk_f32 v174, v157, 0x3a0293ee, v4
	v_fmamk_f32 v175, v158, 0x3a0293ee, v4
	v_fmamk_f32 v176, v159, 0x3a0293ee, v4
	v_fmamk_f32 v177, v160, 0x3a0293ee, v4
	v_fmac_f32_e32 v4, 0x3a0293ee, v161
	v_exp_f32_e32 v156, v5
	v_exp_f32_e32 v157, v6
	v_exp_f32_e32 v12, v7
	v_exp_f32_e32 v14, v8
	v_exp_f32_e32 v146, v11
	v_exp_f32_e32 v11, v166
	v_exp_f32_e32 v8, v167
	v_exp_f32_e32 v166, v169
	v_exp_f32_e32 v167, v170
	v_exp_f32_e32 v160, v148
	v_exp_f32_e32 v161, v149
	v_exp_f32_e32 v152, v9
	v_exp_f32_e32 v147, v13
	v_exp_f32_e32 v13, v15
	v_exp_f32_e32 v15, v162
	v_exp_f32_e32 v7, v164
	v_exp_f32_e32 v164, v150
	v_exp_f32_e32 v162, v171
	v_exp_f32_e32 v153, v10
	v_exp_f32_e32 v6, v163
	v_exp_f32_e32 v10, v165
	v_exp_f32_e32 v165, v151
	v_exp_f32_e32 v163, v172
	v_exp_f32_e32 v158, v154
	v_exp_f32_e32 v148, v173
	v_exp_f32_e32 v9, v168
	v_exp_f32_e32 v159, v155
	v_exp_f32_e32 v149, v174
	v_exp_f32_e32 v151, v4
	v_exp_f32_e32 v154, v175
	v_exp_f32_e32 v150, v177
	v_exp_f32_e32 v155, v176
	s_setprio 0
	s_mov_b64 s[6:7], -1
	s_and_b64 vcc, exec, s[70:71]
	s_cbranch_vccz .LBB0_1279
	s_waitcnt vmcnt(0) lgkmcnt(0)
	s_mov_b64 s[6:7], 0

; __device__ __forceinline__ void finishSM8(f32x16& p0, f32x16& p1, float alpha, float& l_reg, i32x8& pa) {
;     for (int r = 0; r < 16; ++r) p1[r] = __builtin_amdgcn_exp2f(p1[r]);
;     float ps;
;     { float s0 = p0[0] + p0[1], s1 = p0[2] + p0[3], s2 = p1[0] + p1[1], s3 = p1[2] + p1[3];
; #pragma unroll
;       for (int r = 4; r < 16; r += 4) { s0 += p0[r]; s0 += p0[r + 1]; s1 += p0[r + 2]; s1 += p0[r + 3]; s2 += p1[r]; s2 += p1[r + 1]; s3 += p1[r + 2]; s3 += p1[r + 3]; }
;       ps = (s0 + s1) + (s2 + s3); }
;     { auto rr = __builtin_amdgcn_permlane32_swap(__float_as_uint(ps), __float_as_uint(ps), false, false);
;       ps = __uint_as_float(rr[0]) + __uint_as_float(rr[1]); }
;     l_reg = l_reg * alpha + ps;
; #pragma unroll
;     for (int d = 0; d < 4; ++d) { int w0 = 0, w1 = 0;
;         w0 = __builtin_amdgcn_cvt_pk_fp8_f32(p0[4 * d], p0[4 * d + 1], w0, false); w0 = __builtin_amdgcn_cvt_pk_fp8_f32(p0[4 * d + 2], p0[4 * d + 3], w0, true);
;         w1 = __builtin_amdgcn_cvt_pk_fp8_f32(p1[4 * d], p1[4 * d + 1], w1, false); w1 = __builtin_amdgcn_cvt_pk_fp8_f32(p1[4 * d + 2], p1[4 * d + 3], w1, true);
;         pa[d] = w0; pa[4 + d] = w1; }
.LBB0_1283:
	v_add_f32_e32 v4, v156, v157
	v_add_f32_e32 v5, v12, v14
	v_add_f32_e32 v168, v166, v167
	v_add_f32_e32 v169, v160, v161
	v_add_f32_e32 v4, v152, v4
	v_add_f32_e32 v5, v146, v5
	v_add_f32_e32 v168, v164, v168
	v_add_f32_e32 v169, v162, v169
	v_add_f32_e32 v4, v153, v4
	v_add_f32_e32 v5, v147, v5
	v_add_f32_e32 v168, v165, v168
	v_add_f32_e32 v169, v163, v169
	v_add_f32_e32 v4, v13, v4
	v_add_f32_e32 v5, v6, v5
	v_add_f32_e32 v168, v158, v168
	v_add_f32_e32 v169, v148, v169
	v_add_f32_e32 v4, v15, v4
	v_add_f32_e32 v5, v7, v5
	v_add_f32_e32 v168, v159, v168
	v_add_f32_e32 v169, v149, v169
	v_add_f32_e32 v4, v10, v4
	v_add_f32_e32 v5, v8, v5
	v_add_f32_e32 v168, v154, v168
	v_add_f32_e32 v169, v150, v169
	v_add_f32_e32 v4, v11, v4
	v_add_f32_e32 v5, v9, v5
	v_add_f32_e32 v168, v155, v168
	v_add_f32_e32 v169, v151, v169
	v_add_f32_e32 v4, v5, v4
	v_add_f32_e32 v5, v168, v169
	v_add_f32_e32 v4, v5, v4
	v_mov_b32_e32 v5, v4
	s_nop 1
	v_permlane32_swap_b32_e32 v4, v5
	v_mov_b32_e32 v168, 0
	v_mov_b32_e32 v172, 0
	v_mov_b32_e32 v169, 0
	v_mov_b32_e32 v173, 0
	v_mov_b32_e32 v170, 0
	v_mov_b32_e32 v174, 0
	v_mov_b32_e32 v171, 0
	v_mov_b32_e32 v175, 0
	v_cvt_pk_fp8_f32 v168, v156, v157
	v_cvt_pk_fp8_f32 v172, v166, v167
	v_cvt_pk_fp8_f32 v169, v152, v153
	v_cvt_pk_fp8_f32 v173, v164, v165
	v_cvt_pk_fp8_f32 v170, v13, v15
	v_cvt_pk_fp8_f32 v174, v158, v159
	v_cvt_pk_fp8_f32 v171, v10, v11
	v_cvt_pk_fp8_f32 v175, v154, v155
	v_cvt_pk_fp8_f32 v168, v12, v14 op_sel:[0,0,1]
	v_cvt_pk_fp8_f32 v172, v160, v161 op_sel:[0,0,1]
	v_cvt_pk_fp8_f32 v169, v146, v147 op_sel:[0,0,1]
	v_cvt_pk_fp8_f32 v173, v162, v163 op_sel:[0,0,1]
	v_cvt_pk_fp8_f32 v170, v6, v7 op_sel:[0,0,1]
	v_cvt_pk_fp8_f32 v174, v148, v149 op_sel:[0,0,1]
	v_cvt_pk_fp8_f32 v171, v8, v9 op_sel:[0,0,1]
	v_cvt_pk_fp8_f32 v175, v150, v151 op_sel:[0,0,1]
	ds_read_b128 v[6:9], v203 offset:32768
	ds_read_b128 v[146:149], v203 offset:34816
	ds_read_b128 v[10:13], v214 offset:32768
	ds_read_b128 v[150:153], v214 offset:34816
	s_waitcnt lgkmcnt(0)
	v_mfma_f32_32x32x64_f8f6f4 v[130:145], v[168:175], v[6:13], v[130:145]
	ds_read_b128 v[6:9], v203 offset:36864
	ds_read_b128 v[10:13], v214 offset:36864
	v_mfma_f32_32x32x64_f8f6f4 v[114:129], v[168:175], v[146:153], v[114:129]
	ds_read_b128 v[146:149], v203 offset:38912
	ds_read_b128 v[150:153], v214 offset:38912
	s_waitcnt lgkmcnt(0)
	v_mfma_f32_32x32x64_f8f6f4 v[98:113], v[168:175], v[6:13], v[98:113]
	ds_read_b128 v[6:9], v203 offset:49152
	ds_read_b128 v[10:13], v214 offset:49152
	v_mfma_f32_32x32x64_f8f6f4 v[82:97], v[168:175], v[146:153], v[82:97]
	ds_read_b128 v[146:149], v203 offset:51200
	ds_read_b128 v[150:153], v214 offset:51200
	s_waitcnt lgkmcnt(0)
	v_mfma_f32_32x32x64_f8f6f4 v[66:81], v[168:175], v[6:13], v[66:81]
	ds_read_b128 v[6:9], v203 offset:53248
	ds_read_b128 v[10:13], v214 offset:53248
	v_mfma_f32_32x32x64_f8f6f4 v[50:65], v[168:175], v[146:153], v[50:65]
	ds_read_b128 v[146:149], v203 offset:55296
	ds_read_b128 v[150:153], v214 offset:55296
	s_waitcnt lgkmcnt(0)
	v_mfma_f32_32x32x64_f8f6f4 v[34:49], v[168:175], v[6:13], v[34:49]
	v_mfma_f32_32x32x64_f8f6f4 v[18:33], v[168:175], v[146:153], v[18:33]
	s_nop 15
	s_nop 15
	s_mov_b64 s[6:7], -1
	s_and_b64 vcc, exec, s[70:71]
	s_cbranch_vccz .LBB0_1285
	s_waitcnt vmcnt(0) lgkmcnt(0)
	s_mov_b64 s[6:7], 0

; __global__ void __launch_bounds__(NWAVES * 64, 2) mk_fwd(Args args) {
	.amdhsa_kernel _Z6mk_fwd4Args
		.amdhsa_group_segment_fixed_size 0
		.amdhsa_private_segment_fixed_size 0
		.amdhsa_kernarg_size 440
		.amdhsa_user_sgpr_count 2
		.amdhsa_user_sgpr_dispatch_ptr 0
		.amdhsa_user_sgpr_queue_ptr 0
		.amdhsa_user_sgpr_kernarg_segment_ptr 1
		.amdhsa_user_sgpr_dispatch_id 0
		.amdhsa_user_sgpr_kernarg_preload_length 0
		.amdhsa_user_sgpr_kernarg_preload_offset 0
		.amdhsa_user_sgpr_private_segment_size 0
		.amdhsa_uses_dynamic_stack 0
		.amdhsa_enable_private_segment 0
		.amdhsa_system_sgpr_workgroup_id_x 1
		.amdhsa_system_sgpr_workgroup_id_y 0
		.amdhsa_system_sgpr_workgroup_id_z 0
		.amdhsa_system_sgpr_workgroup_info 0
		.amdhsa_system_vgpr_workitem_id 0
		.amdhsa_next_free_vgpr 256
		.amdhsa_next_free_sgpr 102
		.amdhsa_accum_offset 256
		.amdhsa_reserve_vcc 1
		.amdhsa_float_round_mode_32 0
		.amdhsa_float_round_mode_16_64 0
		.amdhsa_float_denorm_mode_32 3
		.amdhsa_float_denorm_mode_16_64 3
		.amdhsa_dx10_clamp 1
		.amdhsa_ieee_mode 1
		.amdhsa_fp16_overflow 0
		.amdhsa_tg_split 0
		.amdhsa_exception_fp_ieee_invalid_op 0
		.amdhsa_exception_fp_denorm_src 0
		.amdhsa_exception_fp_ieee_div_zero 0
		.amdhsa_exception_fp_ieee_overflow 0
		.amdhsa_exception_fp_ieee_underflow 0
		.amdhsa_exception_fp_ieee_inexact 0
		.amdhsa_exception_int_div_zero 0
	.end_amdhsa_kernel

; __global__ void __launch_bounds__(NWAVES * 64, 2) mk_fwd(Args args) {
amdhsa.kernels:
  - .agpr_count:     0
    .args:
      - .offset:         0
        .size:           184
        .value_kind:     by_value
      - .offset:         184
        .size:           4
        .value_kind:     hidden_block_count_x
      - .offset:         188
        .size:           4
        .value_kind:     hidden_block_count_y
      - .offset:         192
        .size:           4
        .value_kind:     hidden_block_count_z
      - .offset:         196
        .size:           2
        .value_kind:     hidden_group_size_x
      - .offset:         198
        .size:           2
        .value_kind:     hidden_group_size_y
      - .offset:         200
        .size:           2
        .value_kind:     hidden_group_size_z
      - .offset:         202
        .size:           2
        .value_kind:     hidden_remainder_x
      - .offset:         204
        .size:           2
        .value_kind:     hidden_remainder_y
      - .offset:         206
        .size:           2
        .value_kind:     hidden_remainder_z
      - .offset:         224
        .size:           8
        .value_kind:     hidden_global_offset_x
      - .offset:         232
        .size:           8
        .value_kind:     hidden_global_offset_y
      - .offset:         240
        .size:           8
        .value_kind:     hidden_global_offset_z
      - .offset:         248
        .size:           2
        .value_kind:     hidden_grid_dims
      - .offset:         304
        .size:           4
        .value_kind:     hidden_dynamic_lds_size
    .group_segment_fixed_size: 0
    .kernarg_segment_align: 8
    .kernarg_segment_size: 440
    .language:       OpenCL C
    .language_version:
      - 2
      - 0
    .max_flat_workgroup_size: 512
    .name:           _Z6mk_fwd4Args
    .private_segment_fixed_size: 0
    .sgpr_count:     108
    .sgpr_spill_count: 117
    .symbol:         _Z6mk_fwd4Args.kd
    .uniform_work_group_size: 1
    .uses_dynamic_stack: false
    .vgpr_count:     256
    .vgpr_spill_count: 0
    .wavefront_size: 64
